# v58 + M3 (GLA outputs) gating stage rewritten by hand in both layers: 8 gate lane-permutes issued together, batched silu, 8 store permutes together instead of 16 dependent LDS round trips (bit-identic
# speedup vs baseline: 1.0004x; 1.0004x over previous
; __device__ __forceinline__ unsigned cvt_pk_bf16(float lo, float hi) { const f32x2c_t v = {lo, hi}; return __builtin_bit_cast(unsigned, __builtin_convertvector(v, bf16x2c_t)); }
; __device__ __forceinline__ float silu_f(float a) { return a * __builtin_amdgcn_rcpf(1.0f + __builtin_amdgcn_exp2f(a * -1.4426950408889634f)); }
; __device__ __forceinline__ pg8::u32x2 lane_perm2(pg8::u32x2 w, int src4) { pg8::u32x2 r; r.x = (unsigned)__builtin_amdgcn_ds_bpermute(src4, (int)w.x); r.y = (unsigned)__builtin_amdgcn_ds_bpermute(src4, (int)w.y); return r; }
; template <int layer> __device__ __forceinline__ void layer_phases(const Ctx& c, unsigned char* lds) {
;     ...
;                   const float rs = __builtin_amdgcn_rsqf((rsq[(tt * 2) * 16 + ql] + rsq[(tt * 2 + 1) * 16 + ql]) * (1.0f / 128.0f) + pg8::RMS_EPS);
; #pragma unroll
;                   for (int vt = 0; vt < 4; ++vt) { const int v0 = 16 * (4 * vh + vt) + 4 * g4;
;                       const int t2 = 16 * tt + (lane >> 2), v2 = 16 * (4 * vh + vt) + 4 * (lane & 3);
;                       const pg8::u32x2 gr = lane_perm2(grv[vt], QSRC_LD(lane)); const f32x4 gv = gnv[vt];
;                       const float o0 = acc[vt][0] * rs * gv[0] * pg8::silu_f(bflo(gr.x)), o1 = acc[vt][1] * rs * gv[1] * pg8::silu_f(bfhi(gr.x));
;                       const float o2 = acc[vt][2] * rs * gv[2] * pg8::silu_f(bflo(gr.y)), o3 = acc[vt][3] * rs * gv[3] * pg8::silu_f(bfhi(gr.y));
;                       pg8::u32x2 w; w.x = pg8::cvt_pk_bf16(o0, o1); w.y = pg8::cvt_pk_bf16(o2, o3);
;                       *(pg8::u32x2*)(MIX + (row0 + t2) * D + 256 + h * 128 + v2) = lane_perm2(w, QSRC_ST(lane)); } }
;                 M3_LOADS_G(un);
.LBB0_549:
	s_or_b64 exec, exec, s[80:81]
	s_waitcnt vmcnt(10)
	ds_bpermute_b32 v134, v112, v110
	ds_bpermute_b32 v135, v112, v111
	ds_bpermute_b32 v136, v112, v108
	ds_bpermute_b32 v137, v112, v109
	ds_bpermute_b32 v138, v112, v106
	ds_bpermute_b32 v139, v112, v107
	ds_bpermute_b32 v140, v112, v104
	ds_bpermute_b32 v141, v112, v105
	s_waitcnt lgkmcnt(0)
	s_barrier
	ds_read2_b32 v[132:133], v97 offset1:16
	s_ashr_i32 s80, s83, 7
	s_ashr_i32 s81, s80, 31
	s_and_b32 s83, s2, 0x7c0
	s_lshl_b64 s[80:81], s[80:81], 11
	s_or_b32 s80, s80, s83
	v_mov_b32_e32 v191, s81
	v_or_b32_e32 v190, s80, v96
	v_lshlrev_b64 v[190:191], 11, v[190:191]
	s_and_b32 s80, s84, 0x180
	v_lshl_add_u64 v[190:191], s[46:47], 0, v[190:191]
	s_lshl_b32 s80, s80, 1
	s_mov_b32 s81, s59
	v_lshl_add_u64 v[190:191], v[190:191], 0, s[80:81]
	v_mov_b32_e32 v99, v89
	v_lshl_add_u64 v[194:195], v[190:191], 0, v[98:99]
	v_mov_b32_e32 v101, v89
	s_mul_i32 s80, s49, 0x1800
	s_lshl_b32 s58, s58, 1
	s_mov_b32 s83, s59
	v_mov_b32_e32 v103, v89
	s_add_i32 s84, s84, s85
	s_andn2_b64 vcc, exec, s[56:57]
	v_lshl_add_u64 v[180:181], v[190:191], 0, v[100:101]
	v_lshlrev_b32_e32 v142, 16, v134
	v_and_b32_e32 v143, 0xffff0000, v134
	v_lshlrev_b32_e32 v144, 16, v135
	v_and_b32_e32 v145, 0xffff0000, v135
	v_lshlrev_b32_e32 v146, 16, v136
	v_and_b32_e32 v147, 0xffff0000, v136
	v_lshlrev_b32_e32 v148, 16, v137
	v_and_b32_e32 v149, 0xffff0000, v137
	v_lshlrev_b32_e32 v150, 16, v138
	v_and_b32_e32 v151, 0xffff0000, v138
	v_lshlrev_b32_e32 v152, 16, v139
	v_and_b32_e32 v153, 0xffff0000, v139
	v_lshlrev_b32_e32 v154, 16, v140
	v_and_b32_e32 v155, 0xffff0000, v140
	v_lshlrev_b32_e32 v156, 16, v141
	v_and_b32_e32 v157, 0xffff0000, v141
	v_mul_f32_e32 v158, 0xbfb8aa3b, v142
	v_mul_f32_e32 v159, 0xbfb8aa3b, v143
	v_mul_f32_e32 v160, 0xbfb8aa3b, v144
	v_mul_f32_e32 v161, 0xbfb8aa3b, v145
	v_mul_f32_e32 v162, 0xbfb8aa3b, v146
	v_mul_f32_e32 v163, 0xbfb8aa3b, v147
	v_mul_f32_e32 v164, 0xbfb8aa3b, v148
	v_mul_f32_e32 v165, 0xbfb8aa3b, v149
	v_mul_f32_e32 v166, 0xbfb8aa3b, v150
	v_mul_f32_e32 v167, 0xbfb8aa3b, v151
	v_mul_f32_e32 v168, 0xbfb8aa3b, v152
	v_mul_f32_e32 v169, 0xbfb8aa3b, v153
	v_mul_f32_e32 v170, 0xbfb8aa3b, v154
	v_mul_f32_e32 v171, 0xbfb8aa3b, v155
	v_mul_f32_e32 v172, 0xbfb8aa3b, v156
	v_mul_f32_e32 v173, 0xbfb8aa3b, v157
	v_exp_f32_e32 v158, v158
	v_exp_f32_e32 v159, v159
	v_exp_f32_e32 v160, v160
	v_exp_f32_e32 v161, v161
	v_exp_f32_e32 v162, v162
	v_exp_f32_e32 v163, v163
	v_exp_f32_e32 v164, v164
	v_exp_f32_e32 v165, v165
	v_exp_f32_e32 v166, v166
	v_exp_f32_e32 v167, v167
	v_exp_f32_e32 v168, v168
	v_exp_f32_e32 v169, v169
	v_exp_f32_e32 v170, v170
	v_exp_f32_e32 v171, v171
	v_exp_f32_e32 v172, v172
	v_exp_f32_e32 v173, v173
	v_add_f32_e32 v158, 1.0, v158
	v_add_f32_e32 v159, 1.0, v159
	v_add_f32_e32 v160, 1.0, v160
	v_add_f32_e32 v161, 1.0, v161
	v_add_f32_e32 v162, 1.0, v162
	v_add_f32_e32 v163, 1.0, v163
	v_add_f32_e32 v164, 1.0, v164
	v_add_f32_e32 v165, 1.0, v165
	v_add_f32_e32 v166, 1.0, v166
	v_add_f32_e32 v167, 1.0, v167
	v_add_f32_e32 v168, 1.0, v168
	v_add_f32_e32 v169, 1.0, v169
	v_add_f32_e32 v170, 1.0, v170
	v_add_f32_e32 v171, 1.0, v171
	v_add_f32_e32 v172, 1.0, v172
	v_add_f32_e32 v173, 1.0, v173
	v_rcp_f32_e32 v158, v158
	v_rcp_f32_e32 v159, v159
	v_rcp_f32_e32 v160, v160
	v_rcp_f32_e32 v161, v161
	v_rcp_f32_e32 v162, v162
	v_rcp_f32_e32 v163, v163
	v_rcp_f32_e32 v164, v164
	v_rcp_f32_e32 v165, v165
	v_rcp_f32_e32 v166, v166
	v_rcp_f32_e32 v167, v167
	v_rcp_f32_e32 v168, v168
	v_rcp_f32_e32 v169, v169
	v_rcp_f32_e32 v170, v170
	v_rcp_f32_e32 v171, v171
	v_rcp_f32_e32 v172, v172
	v_rcp_f32_e32 v173, v173
	v_pk_mul_f32 v[158:159], v[158:159], v[142:143]
	v_pk_mul_f32 v[160:161], v[160:161], v[144:145]
	v_pk_mul_f32 v[162:163], v[162:163], v[146:147]
	v_pk_mul_f32 v[164:165], v[164:165], v[148:149]
	v_pk_mul_f32 v[166:167], v[166:167], v[150:151]
	v_pk_mul_f32 v[168:169], v[168:169], v[152:153]
	v_pk_mul_f32 v[170:171], v[170:171], v[154:155]
	v_pk_mul_f32 v[172:173], v[172:173], v[156:157]
	s_waitcnt lgkmcnt(0)
	v_add_f32_e32 v132, v132, v133
	v_fmamk_f32 v132, v132, 0x3c000000, v124
	v_rsq_f32_e32 v176, v132
	s_nop 0
	v_pk_mul_f32 v[74:75], v[74:75], v[176:177] op_sel_hi:[1,0]
	v_pk_mul_f32 v[76:77], v[76:77], v[176:177] op_sel_hi:[1,0]
	v_pk_mul_f32 v[66:67], v[66:67], v[176:177] op_sel_hi:[1,0]
	v_pk_mul_f32 v[68:69], v[68:69], v[176:177] op_sel_hi:[1,0]
	v_pk_mul_f32 v[62:63], v[62:63], v[176:177] op_sel_hi:[1,0]
	v_pk_mul_f32 v[64:65], v[64:65], v[176:177] op_sel_hi:[1,0]
	v_pk_mul_f32 v[58:59], v[58:59], v[176:177] op_sel_hi:[1,0]
	v_pk_mul_f32 v[60:61], v[60:61], v[176:177] op_sel_hi:[1,0]
	v_pk_mul_f32 v[74:75], v[14:15], v[74:75]
	v_pk_mul_f32 v[76:77], v[16:17], v[76:77]
	v_pk_mul_f32 v[66:67], v[6:7], v[66:67]
	v_pk_mul_f32 v[68:69], v[8:9], v[68:69]
	v_pk_mul_f32 v[62:63], v[2:3], v[62:63]
	v_pk_mul_f32 v[64:65], v[4:5], v[64:65]
	v_pk_mul_f32 v[58:59], v[10:11], v[58:59]
	v_pk_mul_f32 v[60:61], v[12:13], v[60:61]
	v_pk_mul_f32 v[74:75], v[74:75], v[158:159]
	v_pk_mul_f32 v[76:77], v[76:77], v[160:161]
	v_pk_mul_f32 v[66:67], v[66:67], v[162:163]
	v_pk_mul_f32 v[68:69], v[68:69], v[164:165]
	v_pk_mul_f32 v[62:63], v[62:63], v[166:167]
	v_pk_mul_f32 v[64:65], v[64:65], v[168:169]
	v_pk_mul_f32 v[58:59], v[58:59], v[170:171]
	v_pk_mul_f32 v[60:61], v[60:61], v[172:173]
	v_cvt_pk_bf16_f32 v134, v74, v75
	v_cvt_pk_bf16_f32 v135, v76, v77
	v_cvt_pk_bf16_f32 v136, v66, v67
	v_cvt_pk_bf16_f32 v137, v68, v69
	v_cvt_pk_bf16_f32 v138, v62, v63
	v_cvt_pk_bf16_f32 v139, v64, v65
	v_cvt_pk_bf16_f32 v140, v58, v59
	v_cvt_pk_bf16_f32 v141, v60, v61
	ds_bpermute_b32 v142, v113, v134
	ds_bpermute_b32 v143, v113, v135
	ds_bpermute_b32 v144, v113, v136
	ds_bpermute_b32 v145, v113, v137
	ds_bpermute_b32 v146, v113, v138
	ds_bpermute_b32 v147, v113, v139
	ds_bpermute_b32 v148, v113, v140
	ds_bpermute_b32 v149, v113, v141
	s_waitcnt lgkmcnt(0)
	global_store_dwordx2 v[194:195], v[142:143], off offset:512
	global_store_dwordx2 v[194:195], v[144:145], off offset:544
	global_store_dwordx2 v[194:195], v[146:147], off offset:576
	global_store_dwordx2 v[180:181], v[148:149], off offset:512
	v_or_b32_e32 v180, s48, v96
	v_mov_b64_e32 v[178:179], s[44:45]
	v_mad_u64_u32 v[178:179], s[48:49], v180, s3, v[178:179]
	v_add_u32_e32 v179, s80, v179
	v_lshl_add_u64 v[178:179], v[178:179], 0, s[58:59]
	v_lshl_add_u64 v[178:179], v[178:179], 0, s[82:83]
	v_lshl_add_u64 v[178:179], v[178:179], 0, v[102:103]
	global_load_dwordx2 v[110:111], v[178:179], off offset:3584
	global_load_dwordx2 v[108:109], v[178:179], off offset:3616
	global_load_dwordx2 v[106:107], v[178:179], off offset:3648
	global_load_dwordx2 v[104:105], v[178:179], off offset:3680
	v_readlane_b32 s48, v255, 23
	s_add_i32 s2, s2, s48
	s_mov_b32 s83, s88
	s_barrier
	v_readlane_b32 s49, v255, 24
	s_cbranch_vccz .LBB0_559

; __device__ __forceinline__ unsigned cvt_pk_bf16(float lo, float hi) { const f32x2c_t v = {lo, hi}; return __builtin_bit_cast(unsigned, __builtin_convertvector(v, bf16x2c_t)); }
; __device__ __forceinline__ float silu_f(float a) { return a * __builtin_amdgcn_rcpf(1.0f + __builtin_amdgcn_exp2f(a * -1.4426950408889634f)); }
; __device__ __forceinline__ pg8::u32x2 lane_perm2(pg8::u32x2 w, int src4) { pg8::u32x2 r; r.x = (unsigned)__builtin_amdgcn_ds_bpermute(src4, (int)w.x); r.y = (unsigned)__builtin_amdgcn_ds_bpermute(src4, (int)w.y); return r; }
; template <int layer> __device__ __forceinline__ void layer_phases(const Ctx& c, unsigned char* lds) {
;     ...
;                   const float rs = __builtin_amdgcn_rsqf((rsq[(tt * 2) * 16 + ql] + rsq[(tt * 2 + 1) * 16 + ql]) * (1.0f / 128.0f) + pg8::RMS_EPS);
; #pragma unroll
;                   for (int vt = 0; vt < 4; ++vt) { const int v0 = 16 * (4 * vh + vt) + 4 * g4;
;                       const int t2 = 16 * tt + (lane >> 2), v2 = 16 * (4 * vh + vt) + 4 * (lane & 3);
;                       const pg8::u32x2 gr = lane_perm2(grv[vt], QSRC_LD(lane)); const f32x4 gv = gnv[vt];
;                       const float o0 = acc[vt][0] * rs * gv[0] * pg8::silu_f(bflo(gr.x)), o1 = acc[vt][1] * rs * gv[1] * pg8::silu_f(bfhi(gr.x));
;                       const float o2 = acc[vt][2] * rs * gv[2] * pg8::silu_f(bflo(gr.y)), o3 = acc[vt][3] * rs * gv[3] * pg8::silu_f(bfhi(gr.y));
;                       pg8::u32x2 w; w.x = pg8::cvt_pk_bf16(o0, o1); w.y = pg8::cvt_pk_bf16(o2, o3);
;                       *(pg8::u32x2*)(MIX + (row0 + t2) * D + 256 + h * 128 + v2) = lane_perm2(w, QSRC_ST(lane)); } }
;                 M3_LOADS_G(un);
.LBB0_1240:
	s_or_b64 exec, exec, s[64:65]
	s_waitcnt vmcnt(10)
	ds_bpermute_b32 v134, v112, v110
	ds_bpermute_b32 v135, v112, v111
	ds_bpermute_b32 v136, v112, v108
	ds_bpermute_b32 v137, v112, v109
	ds_bpermute_b32 v138, v112, v106
	ds_bpermute_b32 v139, v112, v107
	ds_bpermute_b32 v140, v112, v104
	ds_bpermute_b32 v141, v112, v105
	s_waitcnt lgkmcnt(0)
	s_barrier
	ds_read2_b32 v[132:133], v97 offset1:16
	s_ashr_i32 s64, s59, 7
	s_ashr_i32 s65, s64, 31
	s_and_b32 s59, s2, 0x7c0
	s_lshl_b64 s[64:65], s[64:65], 11
	s_or_b32 s59, s64, s59
	v_mov_b32_e32 v195, s65
	v_or_b32_e32 v194, s59, v96
	v_lshlrev_b64 v[194:195], 11, v[194:195]
	s_and_b32 s59, s66, 0x180
	v_lshl_add_u64 v[194:195], s[46:47], 0, v[194:195]
	s_lshl_b32 s64, s59, 1
	s_mov_b32 s65, s41
	v_lshl_add_u64 v[194:195], v[194:195], 0, s[64:65]
	v_mov_b32_e32 v99, v89
	v_lshl_add_u64 v[190:191], v[194:195], 0, v[98:99]
	v_mov_b32_e32 v101, v89
	s_mul_i32 s59, s63, 0x1800
	s_lshl_b32 s40, s40, 1
	v_mov_b32_e32 v103, v89
	s_add_i32 s66, s66, s67
	s_add_i32 s2, s2, s82
	s_andn2_b64 vcc, exec, s[60:61]
	v_lshl_add_u64 v[180:181], v[194:195], 0, v[100:101]
	v_lshlrev_b32_e32 v142, 16, v134
	v_and_b32_e32 v143, 0xffff0000, v134
	v_lshlrev_b32_e32 v144, 16, v135
	v_and_b32_e32 v145, 0xffff0000, v135
	v_lshlrev_b32_e32 v146, 16, v136
	v_and_b32_e32 v147, 0xffff0000, v136
	v_lshlrev_b32_e32 v148, 16, v137
	v_and_b32_e32 v149, 0xffff0000, v137
	v_lshlrev_b32_e32 v150, 16, v138
	v_and_b32_e32 v151, 0xffff0000, v138
	v_lshlrev_b32_e32 v152, 16, v139
	v_and_b32_e32 v153, 0xffff0000, v139
	v_lshlrev_b32_e32 v154, 16, v140
	v_and_b32_e32 v155, 0xffff0000, v140
	v_lshlrev_b32_e32 v156, 16, v141
	v_and_b32_e32 v157, 0xffff0000, v141
	v_mul_f32_e32 v158, 0xbfb8aa3b, v142
	v_mul_f32_e32 v159, 0xbfb8aa3b, v143
	v_mul_f32_e32 v160, 0xbfb8aa3b, v144
	v_mul_f32_e32 v161, 0xbfb8aa3b, v145
	v_mul_f32_e32 v162, 0xbfb8aa3b, v146
	v_mul_f32_e32 v163, 0xbfb8aa3b, v147
	v_mul_f32_e32 v164, 0xbfb8aa3b, v148
	v_mul_f32_e32 v165, 0xbfb8aa3b, v149
	v_mul_f32_e32 v166, 0xbfb8aa3b, v150
	v_mul_f32_e32 v167, 0xbfb8aa3b, v151
	v_mul_f32_e32 v168, 0xbfb8aa3b, v152
	v_mul_f32_e32 v169, 0xbfb8aa3b, v153
	v_mul_f32_e32 v170, 0xbfb8aa3b, v154
	v_mul_f32_e32 v171, 0xbfb8aa3b, v155
	v_mul_f32_e32 v172, 0xbfb8aa3b, v156
	v_mul_f32_e32 v173, 0xbfb8aa3b, v157
	v_exp_f32_e32 v158, v158
	v_exp_f32_e32 v159, v159
	v_exp_f32_e32 v160, v160
	v_exp_f32_e32 v161, v161
	v_exp_f32_e32 v162, v162
	v_exp_f32_e32 v163, v163
	v_exp_f32_e32 v164, v164
	v_exp_f32_e32 v165, v165
	v_exp_f32_e32 v166, v166
	v_exp_f32_e32 v167, v167
	v_exp_f32_e32 v168, v168
	v_exp_f32_e32 v169, v169
	v_exp_f32_e32 v170, v170
	v_exp_f32_e32 v171, v171
	v_exp_f32_e32 v172, v172
	v_exp_f32_e32 v173, v173
	v_add_f32_e32 v158, 1.0, v158
	v_add_f32_e32 v159, 1.0, v159
	v_add_f32_e32 v160, 1.0, v160
	v_add_f32_e32 v161, 1.0, v161
	v_add_f32_e32 v162, 1.0, v162
	v_add_f32_e32 v163, 1.0, v163
	v_add_f32_e32 v164, 1.0, v164
	v_add_f32_e32 v165, 1.0, v165
	v_add_f32_e32 v166, 1.0, v166
	v_add_f32_e32 v167, 1.0, v167
	v_add_f32_e32 v168, 1.0, v168
	v_add_f32_e32 v169, 1.0, v169
	v_add_f32_e32 v170, 1.0, v170
	v_add_f32_e32 v171, 1.0, v171
	v_add_f32_e32 v172, 1.0, v172
	v_add_f32_e32 v173, 1.0, v173
	v_rcp_f32_e32 v158, v158
	v_rcp_f32_e32 v159, v159
	v_rcp_f32_e32 v160, v160
	v_rcp_f32_e32 v161, v161
	v_rcp_f32_e32 v162, v162
	v_rcp_f32_e32 v163, v163
	v_rcp_f32_e32 v164, v164
	v_rcp_f32_e32 v165, v165
	v_rcp_f32_e32 v166, v166
	v_rcp_f32_e32 v167, v167
	v_rcp_f32_e32 v168, v168
	v_rcp_f32_e32 v169, v169
	v_rcp_f32_e32 v170, v170
	v_rcp_f32_e32 v171, v171
	v_rcp_f32_e32 v172, v172
	v_rcp_f32_e32 v173, v173
	v_pk_mul_f32 v[158:159], v[158:159], v[142:143]
	v_pk_mul_f32 v[160:161], v[160:161], v[144:145]
	v_pk_mul_f32 v[162:163], v[162:163], v[146:147]
	v_pk_mul_f32 v[164:165], v[164:165], v[148:149]
	v_pk_mul_f32 v[166:167], v[166:167], v[150:151]
	v_pk_mul_f32 v[168:169], v[168:169], v[152:153]
	v_pk_mul_f32 v[170:171], v[170:171], v[154:155]
	v_pk_mul_f32 v[172:173], v[172:173], v[156:157]
	s_waitcnt lgkmcnt(0)
	v_add_f32_e32 v132, v132, v133
	v_fmamk_f32 v132, v132, 0x3c000000, v124
	v_rsq_f32_e32 v176, v132
	s_nop 0
	v_pk_mul_f32 v[70:71], v[70:71], v[176:177] op_sel_hi:[1,0]
	v_pk_mul_f32 v[72:73], v[72:73], v[176:177] op_sel_hi:[1,0]
	v_pk_mul_f32 v[66:67], v[66:67], v[176:177] op_sel_hi:[1,0]
	v_pk_mul_f32 v[68:69], v[68:69], v[176:177] op_sel_hi:[1,0]
	v_pk_mul_f32 v[62:63], v[62:63], v[176:177] op_sel_hi:[1,0]
	v_pk_mul_f32 v[64:65], v[64:65], v[176:177] op_sel_hi:[1,0]
	v_pk_mul_f32 v[58:59], v[58:59], v[176:177] op_sel_hi:[1,0]
	v_pk_mul_f32 v[60:61], v[60:61], v[176:177] op_sel_hi:[1,0]
	v_pk_mul_f32 v[70:71], v[14:15], v[70:71]
	v_pk_mul_f32 v[72:73], v[16:17], v[72:73]
	v_pk_mul_f32 v[66:67], v[6:7], v[66:67]
	v_pk_mul_f32 v[68:69], v[8:9], v[68:69]
	v_pk_mul_f32 v[62:63], v[2:3], v[62:63]
	v_pk_mul_f32 v[64:65], v[4:5], v[64:65]
	v_pk_mul_f32 v[58:59], v[10:11], v[58:59]
	v_pk_mul_f32 v[60:61], v[12:13], v[60:61]
	v_pk_mul_f32 v[70:71], v[70:71], v[158:159]
	v_pk_mul_f32 v[72:73], v[72:73], v[160:161]
	v_pk_mul_f32 v[66:67], v[66:67], v[162:163]
	v_pk_mul_f32 v[68:69], v[68:69], v[164:165]
	v_pk_mul_f32 v[62:63], v[62:63], v[166:167]
	v_pk_mul_f32 v[64:65], v[64:65], v[168:169]
	v_pk_mul_f32 v[58:59], v[58:59], v[170:171]
	v_pk_mul_f32 v[60:61], v[60:61], v[172:173]
	v_cvt_pk_bf16_f32 v134, v70, v71
	v_cvt_pk_bf16_f32 v135, v72, v73
	v_cvt_pk_bf16_f32 v136, v66, v67
	v_cvt_pk_bf16_f32 v137, v68, v69
	v_cvt_pk_bf16_f32 v138, v62, v63
	v_cvt_pk_bf16_f32 v139, v64, v65
	v_cvt_pk_bf16_f32 v140, v58, v59
	v_cvt_pk_bf16_f32 v141, v60, v61
	ds_bpermute_b32 v142, v113, v134
	ds_bpermute_b32 v143, v113, v135
	ds_bpermute_b32 v144, v113, v136
	ds_bpermute_b32 v145, v113, v137
	ds_bpermute_b32 v146, v113, v138
	ds_bpermute_b32 v147, v113, v139
	ds_bpermute_b32 v148, v113, v140
	ds_bpermute_b32 v149, v113, v141
	s_waitcnt lgkmcnt(0)
	global_store_dwordx2 v[190:191], v[142:143], off offset:512
	global_store_dwordx2 v[190:191], v[144:145], off offset:544
	global_store_dwordx2 v[190:191], v[146:147], off offset:576
	global_store_dwordx2 v[180:181], v[148:149], off offset:512
	v_or_b32_e32 v180, s62, v96
	v_mov_b64_e32 v[178:179], s[44:45]
	v_mad_u64_u32 v[178:179], s[62:63], v180, s3, v[178:179]
	v_add_u32_e32 v179, s59, v179
	v_lshl_add_u64 v[178:179], v[178:179], 0, s[40:41]
	s_mov_b32 s59, s41
	v_lshl_add_u64 v[178:179], v[178:179], 0, s[58:59]
	v_lshl_add_u64 v[178:179], v[178:179], 0, v[102:103]
	global_load_dwordx2 v[110:111], v[178:179], off offset:3584
	global_load_dwordx2 v[108:109], v[178:179], off offset:3616
	global_load_dwordx2 v[106:107], v[178:179], off offset:3648
	global_load_dwordx2 v[104:105], v[178:179], off offset:3680
	s_mov_b32 s59, s68
	s_barrier
	s_cbranch_vccz .LBB0_1250
